# removed hipcc's redundant second accumulator zeroing (128 v_mov per unit) at 5 GEMM sites, on top of K-swizzle
# speedup vs baseline: 1.2463x; 1.2463x over previous
.LBB0_809:
	v_mov_b32_e32 v163, 0
	s_andn2_b64 vcc, exec, s[52:53]
	v_mov_b32_e32 v162, v163
	v_mov_b32_e32 v161, v163
	v_mov_b32_e32 v160, v163
	v_mov_b32_e32 v159, v163
	v_mov_b32_e32 v158, v163
	v_mov_b32_e32 v157, v163
	v_mov_b32_e32 v156, v163
	v_mov_b32_e32 v131, v163
	v_mov_b32_e32 v130, v163
	v_mov_b32_e32 v129, v163
	v_mov_b32_e32 v128, v163
	v_mov_b32_e32 v127, v163
	v_mov_b32_e32 v126, v163
	v_mov_b32_e32 v125, v163
	v_mov_b32_e32 v124, v163
	v_mov_b32_e32 v99, v163
	v_mov_b32_e32 v98, v163
	v_mov_b32_e32 v97, v163
	v_mov_b32_e32 v96, v163
	v_mov_b32_e32 v95, v163
	v_mov_b32_e32 v94, v163
	v_mov_b32_e32 v93, v163
	v_mov_b32_e32 v92, v163
	v_mov_b32_e32 v83, v163
	v_mov_b32_e32 v82, v163
	v_mov_b32_e32 v81, v163
	v_mov_b32_e32 v80, v163
	v_mov_b32_e32 v79, v163
	v_mov_b32_e32 v78, v163
	v_mov_b32_e32 v77, v163
	v_mov_b32_e32 v76, v163
	v_mov_b32_e32 v155, v163
	v_mov_b32_e32 v154, v163
	v_mov_b32_e32 v153, v163
	v_mov_b32_e32 v152, v163
	v_mov_b32_e32 v151, v163
	v_mov_b32_e32 v150, v163
	v_mov_b32_e32 v149, v163
	v_mov_b32_e32 v148, v163
	s_waitcnt vmcnt(0)
	v_mov_b32_e32 v123, v163
	v_mov_b32_e32 v122, v163
	v_mov_b32_e32 v121, v163
	v_mov_b32_e32 v120, v163
	v_mov_b32_e32 v119, v163
	v_mov_b32_e32 v118, v163
	v_mov_b32_e32 v117, v163
	v_mov_b32_e32 v116, v163
	v_mov_b32_e32 v91, v163
	v_mov_b32_e32 v90, v163
	v_mov_b32_e32 v89, v163
	v_mov_b32_e32 v88, v163
	v_mov_b32_e32 v87, v163
	v_mov_b32_e32 v86, v163
	v_mov_b32_e32 v85, v163
	v_mov_b32_e32 v84, v163
	v_mov_b32_e32 v75, v163
	v_mov_b32_e32 v74, v163
	v_mov_b32_e32 v73, v163
	v_mov_b32_e32 v72, v163
	v_mov_b32_e32 v71, v163
	v_mov_b32_e32 v70, v163
	v_mov_b32_e32 v69, v163
	v_mov_b32_e32 v68, v163
	v_mov_b32_e32 v67, v163
	v_mov_b32_e32 v66, v163
	v_mov_b32_e32 v65, v163
	v_mov_b32_e32 v64, v163
	v_mov_b32_e32 v63, v163
	v_mov_b32_e32 v62, v163
	v_mov_b32_e32 v61, v163
	v_mov_b32_e32 v60, v163
	v_mov_b32_e32 v51, v163
	v_mov_b32_e32 v50, v163
	v_mov_b32_e32 v49, v163
	v_mov_b32_e32 v48, v163
	v_mov_b32_e32 v47, v163
	v_mov_b32_e32 v46, v163
	v_mov_b32_e32 v45, v163
	v_mov_b32_e32 v44, v163
	v_mov_b32_e32 v35, v163
	v_mov_b32_e32 v34, v163
	v_mov_b32_e32 v33, v163
	v_mov_b32_e32 v32, v163
	v_mov_b32_e32 v31, v163
	v_mov_b32_e32 v30, v163
	v_mov_b32_e32 v29, v163
	v_mov_b32_e32 v28, v163
	v_mov_b32_e32 v19, v163
	v_mov_b32_e32 v18, v163
	v_mov_b32_e32 v17, v163
	v_mov_b32_e32 v16, v163
	v_mov_b32_e32 v15, v163
	v_mov_b32_e32 v14, v163
	v_mov_b32_e32 v13, v163
	v_mov_b32_e32 v12, v163
	v_mov_b32_e32 v59, v163
	v_mov_b32_e32 v58, v163
	v_mov_b32_e32 v57, v163
	v_mov_b32_e32 v56, v163
	v_mov_b32_e32 v55, v163
	v_mov_b32_e32 v54, v163
	v_mov_b32_e32 v53, v163
	v_mov_b32_e32 v52, v163
	v_mov_b32_e32 v43, v163
	v_mov_b32_e32 v42, v163
	v_mov_b32_e32 v41, v163
	v_mov_b32_e32 v40, v163
	v_mov_b32_e32 v39, v163
	v_mov_b32_e32 v38, v163
	v_mov_b32_e32 v37, v163
	v_mov_b32_e32 v36, v163
	v_mov_b32_e32 v27, v163
	v_mov_b32_e32 v26, v163
	v_mov_b32_e32 v25, v163
	v_mov_b32_e32 v24, v163
	v_mov_b32_e32 v23, v163
	v_mov_b32_e32 v22, v163
	v_mov_b32_e32 v21, v163
	v_mov_b32_e32 v20, v163
	v_mov_b32_e32 v11, v163
	v_mov_b32_e32 v10, v163
	v_mov_b32_e32 v9, v163
	v_mov_b32_e32 v8, v163
	v_mov_b32_e32 v7, v163
	v_mov_b32_e32 v6, v163
	v_mov_b32_e32 v5, v163
	v_mov_b32_e32 v4, v163
	s_cbranch_vccnz .LBB0_812
	s_add_u32 s26, s26, 0x80
	s_addc_u32 s27, s27, 0
	s_add_u32 s19, s30, 0x100
	s_addc_u32 s20, s31, 0
	s_mov_b32 s21, 0

.LBB0_1302:
	v_mov_b32_e32 v127, 0
	s_andn2_b64 vcc, exec, s[42:43]
	v_mov_b32_e32 v126, v127
	v_mov_b32_e32 v125, v127
	v_mov_b32_e32 v124, v127
	v_mov_b32_e32 v131, v127
	v_mov_b32_e32 v130, v127
	v_mov_b32_e32 v129, v127
	v_mov_b32_e32 v128, v127
	v_mov_b32_e32 v115, v127
	v_mov_b32_e32 v114, v127
	v_mov_b32_e32 v113, v127
	v_mov_b32_e32 v112, v127
	v_mov_b32_e32 v111, v127
	v_mov_b32_e32 v110, v127
	v_mov_b32_e32 v109, v127
	v_mov_b32_e32 v108, v127
	v_mov_b32_e32 v99, v127
	v_mov_b32_e32 v98, v127
	v_mov_b32_e32 v97, v127
	v_mov_b32_e32 v96, v127
	v_mov_b32_e32 v95, v127
	v_mov_b32_e32 v94, v127
	v_mov_b32_e32 v93, v127
	v_mov_b32_e32 v92, v127
	v_mov_b32_e32 v83, v127
	v_mov_b32_e32 v82, v127
	v_mov_b32_e32 v81, v127
	v_mov_b32_e32 v80, v127
	v_mov_b32_e32 v79, v127
	v_mov_b32_e32 v78, v127
	v_mov_b32_e32 v77, v127
	v_mov_b32_e32 v76, v127
	v_mov_b32_e32 v123, v127
	v_mov_b32_e32 v122, v127
	v_mov_b32_e32 v121, v127
	v_mov_b32_e32 v120, v127
	v_mov_b32_e32 v119, v127
	v_mov_b32_e32 v118, v127
	v_mov_b32_e32 v117, v127
	v_mov_b32_e32 v116, v127
	v_mov_b32_e32 v107, v127
	v_mov_b32_e32 v106, v127
	v_mov_b32_e32 v105, v127
	v_mov_b32_e32 v104, v127
	v_mov_b32_e32 v103, v127
	v_mov_b32_e32 v102, v127
	v_mov_b32_e32 v101, v127
	v_mov_b32_e32 v100, v127
	v_mov_b32_e32 v91, v127
	v_mov_b32_e32 v90, v127
	v_mov_b32_e32 v89, v127
	v_mov_b32_e32 v88, v127
	v_mov_b32_e32 v87, v127
	v_mov_b32_e32 v86, v127
	v_mov_b32_e32 v85, v127
	v_mov_b32_e32 v84, v127
	v_mov_b32_e32 v75, v127
	v_mov_b32_e32 v74, v127
	v_mov_b32_e32 v73, v127
	v_mov_b32_e32 v72, v127
	v_mov_b32_e32 v71, v127
	v_mov_b32_e32 v70, v127
	v_mov_b32_e32 v69, v127
	v_mov_b32_e32 v68, v127
	v_mov_b32_e32 v67, v127
	v_mov_b32_e32 v66, v127
	v_mov_b32_e32 v65, v127
	v_mov_b32_e32 v64, v127
	v_mov_b32_e32 v63, v127
	v_mov_b32_e32 v62, v127
	v_mov_b32_e32 v61, v127
	v_mov_b32_e32 v60, v127
	v_mov_b32_e32 v51, v127
	v_mov_b32_e32 v50, v127
	v_mov_b32_e32 v49, v127
	v_mov_b32_e32 v48, v127
	v_mov_b32_e32 v47, v127
	v_mov_b32_e32 v46, v127
	v_mov_b32_e32 v45, v127
	v_mov_b32_e32 v44, v127
	v_mov_b32_e32 v35, v127
	v_mov_b32_e32 v34, v127
	v_mov_b32_e32 v33, v127
	v_mov_b32_e32 v32, v127
	v_mov_b32_e32 v31, v127
	v_mov_b32_e32 v30, v127
	v_mov_b32_e32 v29, v127
	v_mov_b32_e32 v28, v127
	v_mov_b32_e32 v19, v127
	v_mov_b32_e32 v18, v127
	v_mov_b32_e32 v17, v127
	v_mov_b32_e32 v16, v127
	v_mov_b32_e32 v15, v127
	v_mov_b32_e32 v14, v127
	v_mov_b32_e32 v13, v127
	v_mov_b32_e32 v12, v127
	v_mov_b32_e32 v59, v127
	v_mov_b32_e32 v58, v127
	v_mov_b32_e32 v57, v127
	v_mov_b32_e32 v56, v127
	v_mov_b32_e32 v55, v127
	v_mov_b32_e32 v54, v127
	v_mov_b32_e32 v53, v127
	v_mov_b32_e32 v52, v127
	v_mov_b32_e32 v43, v127
	v_mov_b32_e32 v42, v127
	v_mov_b32_e32 v41, v127
	v_mov_b32_e32 v40, v127
	v_mov_b32_e32 v39, v127
	v_mov_b32_e32 v38, v127
	v_mov_b32_e32 v37, v127
	v_mov_b32_e32 v36, v127
	v_mov_b32_e32 v27, v127
	v_mov_b32_e32 v26, v127
	v_mov_b32_e32 v25, v127
	v_mov_b32_e32 v24, v127
	v_mov_b32_e32 v23, v127
	v_mov_b32_e32 v22, v127
	v_mov_b32_e32 v21, v127
	v_mov_b32_e32 v20, v127
	v_mov_b32_e32 v11, v127
	v_mov_b32_e32 v10, v127
	v_mov_b32_e32 v9, v127
	v_mov_b32_e32 v8, v127
	v_mov_b32_e32 v7, v127
	v_mov_b32_e32 v6, v127
	v_mov_b32_e32 v5, v127
	v_mov_b32_e32 v4, v127
	s_cbranch_vccnz .LBB0_1305
	s_add_u32 s2, s30, 0x80
	s_addc_u32 s3, s31, 0
	s_add_u32 s19, s26, 0x100
	s_addc_u32 s20, s27, 0
	s_mov_b32 s21, 0

.LBB0_1327:
	v_mov_b32_e32 v131, 0
	s_andn2_b64 vcc, exec, s[16:17]
	v_mov_b32_e32 v130, v131
	v_mov_b32_e32 v129, v131
	v_mov_b32_e32 v128, v131
	v_mov_b32_e32 v127, v131
	v_mov_b32_e32 v126, v131
	v_mov_b32_e32 v125, v131
	v_mov_b32_e32 v124, v131
	v_mov_b32_e32 v115, v131
	v_mov_b32_e32 v114, v131
	v_mov_b32_e32 v113, v131
	v_mov_b32_e32 v112, v131
	v_mov_b32_e32 v111, v131
	v_mov_b32_e32 v110, v131
	v_mov_b32_e32 v109, v131
	v_mov_b32_e32 v108, v131
	v_mov_b32_e32 v99, v131
	v_mov_b32_e32 v98, v131
	v_mov_b32_e32 v97, v131
	v_mov_b32_e32 v96, v131
	v_mov_b32_e32 v95, v131
	v_mov_b32_e32 v94, v131
	v_mov_b32_e32 v93, v131
	v_mov_b32_e32 v92, v131
	v_mov_b32_e32 v83, v131
	v_mov_b32_e32 v82, v131
	v_mov_b32_e32 v81, v131
	v_mov_b32_e32 v80, v131
	v_mov_b32_e32 v79, v131
	v_mov_b32_e32 v78, v131
	v_mov_b32_e32 v77, v131
	v_mov_b32_e32 v76, v131
	v_mov_b32_e32 v123, v131
	v_mov_b32_e32 v122, v131
	v_mov_b32_e32 v121, v131
	v_mov_b32_e32 v120, v131
	v_mov_b32_e32 v119, v131
	v_mov_b32_e32 v118, v131
	v_mov_b32_e32 v117, v131
	v_mov_b32_e32 v116, v131
	v_mov_b32_e32 v107, v131
	v_mov_b32_e32 v106, v131
	v_mov_b32_e32 v105, v131
	v_mov_b32_e32 v104, v131
	v_mov_b32_e32 v103, v131
	v_mov_b32_e32 v102, v131
	v_mov_b32_e32 v101, v131
	v_mov_b32_e32 v100, v131
	v_mov_b32_e32 v91, v131
	v_mov_b32_e32 v90, v131
	v_mov_b32_e32 v89, v131
	v_mov_b32_e32 v88, v131
	v_mov_b32_e32 v87, v131
	v_mov_b32_e32 v86, v131
	v_mov_b32_e32 v85, v131
	v_mov_b32_e32 v84, v131
	v_mov_b32_e32 v75, v131
	v_mov_b32_e32 v74, v131
	v_mov_b32_e32 v73, v131
	v_mov_b32_e32 v72, v131
	v_mov_b32_e32 v71, v131
	v_mov_b32_e32 v70, v131
	v_mov_b32_e32 v69, v131
	v_mov_b32_e32 v68, v131
	v_mov_b32_e32 v67, v131
	v_mov_b32_e32 v66, v131
	v_mov_b32_e32 v65, v131
	v_mov_b32_e32 v64, v131
	v_mov_b32_e32 v63, v131
	v_mov_b32_e32 v62, v131
	v_mov_b32_e32 v61, v131
	v_mov_b32_e32 v60, v131
	v_mov_b32_e32 v51, v131
	v_mov_b32_e32 v50, v131
	v_mov_b32_e32 v49, v131
	v_mov_b32_e32 v48, v131
	v_mov_b32_e32 v47, v131
	v_mov_b32_e32 v46, v131
	v_mov_b32_e32 v45, v131
	v_mov_b32_e32 v44, v131
	v_mov_b32_e32 v35, v131
	v_mov_b32_e32 v34, v131
	v_mov_b32_e32 v33, v131
	v_mov_b32_e32 v32, v131
	v_mov_b32_e32 v31, v131
	v_mov_b32_e32 v30, v131
	v_mov_b32_e32 v29, v131
	v_mov_b32_e32 v28, v131
	v_mov_b32_e32 v19, v131
	v_mov_b32_e32 v18, v131
	v_mov_b32_e32 v17, v131
	v_mov_b32_e32 v16, v131
	v_mov_b32_e32 v15, v131
	v_mov_b32_e32 v14, v131
	v_mov_b32_e32 v13, v131
	v_mov_b32_e32 v12, v131
	v_mov_b32_e32 v59, v131
	v_mov_b32_e32 v58, v131
	v_mov_b32_e32 v57, v131
	v_mov_b32_e32 v56, v131
	v_mov_b32_e32 v55, v131
	v_mov_b32_e32 v54, v131
	v_mov_b32_e32 v53, v131
	v_mov_b32_e32 v52, v131
	v_mov_b32_e32 v43, v131
	v_mov_b32_e32 v42, v131
	v_mov_b32_e32 v41, v131
	v_mov_b32_e32 v40, v131
	v_mov_b32_e32 v39, v131
	v_mov_b32_e32 v38, v131
	v_mov_b32_e32 v37, v131
	v_mov_b32_e32 v36, v131
	v_mov_b32_e32 v27, v131
	v_mov_b32_e32 v26, v131
	v_mov_b32_e32 v25, v131
	v_mov_b32_e32 v24, v131
	v_mov_b32_e32 v23, v131
	v_mov_b32_e32 v22, v131
	v_mov_b32_e32 v21, v131
	v_mov_b32_e32 v20, v131
	v_mov_b32_e32 v11, v131
	v_mov_b32_e32 v10, v131
	v_mov_b32_e32 v9, v131
	v_mov_b32_e32 v8, v131
	s_waitcnt lgkmcnt(0)
	v_mov_b32_e32 v7, v131
	v_mov_b32_e32 v6, v131
	v_mov_b32_e32 v5, v131
	v_mov_b32_e32 v4, v131
	s_cbranch_vccnz .LBB0_1330
	s_add_u32 s2, s30, 0x80
	s_addc_u32 s3, s31, 0
	s_add_u32 s19, s26, 0x100
	s_addc_u32 s20, s27, 0
	s_mov_b32 s21, 0

.LBB0_3265:
	v_mov_b32_e32 v127, 0
	s_andn2_b64 vcc, exec, s[14:15]
	v_mov_b32_e32 v126, v127
	v_mov_b32_e32 v125, v127
	v_mov_b32_e32 v124, v127
	v_mov_b32_e32 v123, v127
	v_mov_b32_e32 v122, v127
	v_mov_b32_e32 v121, v127
	v_mov_b32_e32 v120, v127
	v_mov_b32_e32 v115, v127
	v_mov_b32_e32 v114, v127
	v_mov_b32_e32 v113, v127
	v_mov_b32_e32 v112, v127
	v_mov_b32_e32 v107, v127
	v_mov_b32_e32 v106, v127
	v_mov_b32_e32 v105, v127
	v_mov_b32_e32 v104, v127
	v_mov_b32_e32 v99, v127
	v_mov_b32_e32 v98, v127
	v_mov_b32_e32 v97, v127
	v_mov_b32_e32 v96, v127
	v_mov_b32_e32 v91, v127
	v_mov_b32_e32 v90, v127
	v_mov_b32_e32 v89, v127
	v_mov_b32_e32 v88, v127
	v_mov_b32_e32 v83, v127
	v_mov_b32_e32 v82, v127
	v_mov_b32_e32 v81, v127
	v_mov_b32_e32 v80, v127
	v_mov_b32_e32 v75, v127
	v_mov_b32_e32 v74, v127
	v_mov_b32_e32 v73, v127
	v_mov_b32_e32 v72, v127
	v_mov_b32_e32 v131, v127
	v_mov_b32_e32 v130, v127
	v_mov_b32_e32 v129, v127
	v_mov_b32_e32 v128, v127
	v_mov_b32_e32 v119, v127
	v_mov_b32_e32 v118, v127
	v_mov_b32_e32 v117, v127
	v_mov_b32_e32 v116, v127
	v_mov_b32_e32 v111, v127
	v_mov_b32_e32 v110, v127
	v_mov_b32_e32 v109, v127
	v_mov_b32_e32 v108, v127
	v_mov_b32_e32 v103, v127
	v_mov_b32_e32 v102, v127
	v_mov_b32_e32 v101, v127
	v_mov_b32_e32 v100, v127
	v_mov_b32_e32 v95, v127
	v_mov_b32_e32 v94, v127
	v_mov_b32_e32 v93, v127
	v_mov_b32_e32 v92, v127
	v_mov_b32_e32 v87, v127
	v_mov_b32_e32 v86, v127
	v_mov_b32_e32 v85, v127
	v_mov_b32_e32 v84, v127
	v_mov_b32_e32 v79, v127
	v_mov_b32_e32 v78, v127
	v_mov_b32_e32 v77, v127
	v_mov_b32_e32 v76, v127
	v_mov_b32_e32 v71, v127
	v_mov_b32_e32 v70, v127
	v_mov_b32_e32 v69, v127
	v_mov_b32_e32 v68, v127
	v_mov_b32_e32 v67, v127
	v_mov_b32_e32 v66, v127
	v_mov_b32_e32 v65, v127
	v_mov_b32_e32 v64, v127
	v_mov_b32_e32 v59, v127
	v_mov_b32_e32 v58, v127
	v_mov_b32_e32 v57, v127
	v_mov_b32_e32 v56, v127
	v_mov_b32_e32 v51, v127
	v_mov_b32_e32 v50, v127
	v_mov_b32_e32 v49, v127
	v_mov_b32_e32 v48, v127
	v_mov_b32_e32 v43, v127
	v_mov_b32_e32 v42, v127
	v_mov_b32_e32 v41, v127
	v_mov_b32_e32 v40, v127
	v_mov_b32_e32 v35, v127
	v_mov_b32_e32 v34, v127
	v_mov_b32_e32 v33, v127
	v_mov_b32_e32 v32, v127
	v_mov_b32_e32 v27, v127
	v_mov_b32_e32 v26, v127
	v_mov_b32_e32 v25, v127
	v_mov_b32_e32 v24, v127
	v_mov_b32_e32 v19, v127
	v_mov_b32_e32 v18, v127
	v_mov_b32_e32 v17, v127
	v_mov_b32_e32 v16, v127
	v_mov_b32_e32 v11, v127
	v_mov_b32_e32 v10, v127
	v_mov_b32_e32 v9, v127
	v_mov_b32_e32 v8, v127
	v_mov_b32_e32 v63, v127
	v_mov_b32_e32 v62, v127
	v_mov_b32_e32 v61, v127
	v_mov_b32_e32 v60, v127
	v_mov_b32_e32 v55, v127
	v_mov_b32_e32 v54, v127
	v_mov_b32_e32 v53, v127
	v_mov_b32_e32 v52, v127
	v_mov_b32_e32 v47, v127
	v_mov_b32_e32 v46, v127
	v_mov_b32_e32 v45, v127
	v_mov_b32_e32 v44, v127
	v_mov_b32_e32 v39, v127
	v_mov_b32_e32 v38, v127
	v_mov_b32_e32 v37, v127
	v_mov_b32_e32 v36, v127
	v_mov_b32_e32 v31, v127
	v_mov_b32_e32 v30, v127
	v_mov_b32_e32 v29, v127
	v_mov_b32_e32 v28, v127
	v_mov_b32_e32 v23, v127
	v_mov_b32_e32 v22, v127
	v_mov_b32_e32 v21, v127
	v_mov_b32_e32 v20, v127
	v_mov_b32_e32 v15, v127
	v_mov_b32_e32 v14, v127
	v_mov_b32_e32 v13, v127
	v_mov_b32_e32 v12, v127
	v_mov_b32_e32 v7, v127
	v_mov_b32_e32 v6, v127
	v_mov_b32_e32 v5, v127
	v_mov_b32_e32 v4, v127
	s_cbranch_vccnz .LBB0_3268
	v_mov_b32_e32 v141, v3
	v_mov_b32_e32 v145, v3
	s_add_u32 s19, s26, 0x100
	s_addc_u32 s20, s27, 0
	v_lshl_add_u64 v[148:149], s[36:37], 0, v[140:141]
	v_lshl_add_u64 v[150:151], s[36:37], 0, v[144:145]
	s_mov_b32 s21, 0
	s_mov_b64 s[26:27], 0

.LBB0_3497:
	v_mov_b32_e32 v127, 0
	s_andn2_b64 vcc, exec, s[10:11]
	v_mov_b32_e32 v126, v127
	v_mov_b32_e32 v125, v127
	v_mov_b32_e32 v124, v127
	v_mov_b32_e32 v131, v127
	v_mov_b32_e32 v130, v127
	v_mov_b32_e32 v129, v127
	v_mov_b32_e32 v128, v127
	v_mov_b32_e32 v115, v127
	v_mov_b32_e32 v114, v127
	v_mov_b32_e32 v113, v127
	v_mov_b32_e32 v112, v127
	v_mov_b32_e32 v111, v127
	v_mov_b32_e32 v110, v127
	v_mov_b32_e32 v109, v127
	v_mov_b32_e32 v108, v127
	v_mov_b32_e32 v99, v127
	v_mov_b32_e32 v98, v127
	v_mov_b32_e32 v97, v127
	v_mov_b32_e32 v96, v127
	v_mov_b32_e32 v95, v127
	v_mov_b32_e32 v94, v127
	v_mov_b32_e32 v93, v127
	v_mov_b32_e32 v92, v127
	v_mov_b32_e32 v83, v127
	v_mov_b32_e32 v82, v127
	v_mov_b32_e32 v81, v127
	v_mov_b32_e32 v80, v127
	v_mov_b32_e32 v79, v127
	v_mov_b32_e32 v78, v127
	v_mov_b32_e32 v77, v127
	v_mov_b32_e32 v76, v127
	v_mov_b32_e32 v123, v127
	v_mov_b32_e32 v122, v127
	v_mov_b32_e32 v121, v127
	v_mov_b32_e32 v120, v127
	v_mov_b32_e32 v119, v127
	v_mov_b32_e32 v118, v127
	v_mov_b32_e32 v117, v127
	v_mov_b32_e32 v116, v127
	v_mov_b32_e32 v107, v127
	v_mov_b32_e32 v106, v127
	v_mov_b32_e32 v105, v127
	v_mov_b32_e32 v104, v127
	v_mov_b32_e32 v103, v127
	v_mov_b32_e32 v102, v127
	v_mov_b32_e32 v101, v127
	v_mov_b32_e32 v100, v127
	v_mov_b32_e32 v91, v127
	v_mov_b32_e32 v90, v127
	v_mov_b32_e32 v89, v127
	v_mov_b32_e32 v88, v127
	v_mov_b32_e32 v87, v127
	v_mov_b32_e32 v86, v127
	v_mov_b32_e32 v85, v127
	v_mov_b32_e32 v84, v127
	v_mov_b32_e32 v75, v127
	v_mov_b32_e32 v74, v127
	v_mov_b32_e32 v73, v127
	v_mov_b32_e32 v72, v127
	v_mov_b32_e32 v71, v127
	v_mov_b32_e32 v70, v127
	v_mov_b32_e32 v69, v127
	v_mov_b32_e32 v68, v127
	v_mov_b32_e32 v67, v127
	v_mov_b32_e32 v66, v127
	v_mov_b32_e32 v65, v127
	v_mov_b32_e32 v64, v127
	v_mov_b32_e32 v63, v127
	v_mov_b32_e32 v62, v127
	v_mov_b32_e32 v61, v127
	v_mov_b32_e32 v60, v127
	v_mov_b32_e32 v51, v127
	v_mov_b32_e32 v50, v127
	v_mov_b32_e32 v49, v127
	v_mov_b32_e32 v48, v127
	v_mov_b32_e32 v47, v127
	v_mov_b32_e32 v46, v127
	v_mov_b32_e32 v45, v127
	v_mov_b32_e32 v44, v127
	v_mov_b32_e32 v35, v127
	v_mov_b32_e32 v34, v127
	v_mov_b32_e32 v33, v127
	v_mov_b32_e32 v32, v127
	v_mov_b32_e32 v31, v127
	v_mov_b32_e32 v30, v127
	v_mov_b32_e32 v29, v127
	v_mov_b32_e32 v28, v127
	v_mov_b32_e32 v19, v127
	v_mov_b32_e32 v18, v127
	v_mov_b32_e32 v17, v127
	v_mov_b32_e32 v16, v127
	v_mov_b32_e32 v15, v127
	v_mov_b32_e32 v14, v127
	v_mov_b32_e32 v13, v127
	v_mov_b32_e32 v12, v127
	v_mov_b32_e32 v59, v127
	v_mov_b32_e32 v58, v127
	v_mov_b32_e32 v57, v127
	v_mov_b32_e32 v56, v127
	v_mov_b32_e32 v55, v127
	v_mov_b32_e32 v54, v127
	v_mov_b32_e32 v53, v127
	v_mov_b32_e32 v52, v127
	v_mov_b32_e32 v43, v127
	v_mov_b32_e32 v42, v127
	v_mov_b32_e32 v41, v127
	v_mov_b32_e32 v40, v127
	v_mov_b32_e32 v39, v127
	v_mov_b32_e32 v38, v127
	v_mov_b32_e32 v37, v127
	v_mov_b32_e32 v36, v127
	v_mov_b32_e32 v27, v127
	v_mov_b32_e32 v26, v127
	v_mov_b32_e32 v25, v127
	v_mov_b32_e32 v24, v127
	v_mov_b32_e32 v23, v127
	v_mov_b32_e32 v22, v127
	v_mov_b32_e32 v21, v127
	v_mov_b32_e32 v20, v127
	v_mov_b32_e32 v11, v127
	v_mov_b32_e32 v10, v127
	v_mov_b32_e32 v9, v127
	v_mov_b32_e32 v8, v127
	v_mov_b32_e32 v7, v127
	v_mov_b32_e32 v6, v127
	v_mov_b32_e32 v5, v127
	v_mov_b32_e32 v4, v127
	s_cbranch_vccnz .LBB0_3500
	s_add_u32 s26, s26, 0x80
	s_addc_u32 s27, s27, 0
	s_add_u32 s19, s30, 0x100
	s_addc_u32 s20, s31, 0
	s_mov_b32 s21, 0
